# v49 + per-workgroup code histogram through LDS atomics instead of 16 compares per code after the last barrier
# speedup vs baseline: 1.0188x; 1.0009x over previous
_Z7vq_mainPKfPKiS0_PfPhPdPi:
	s_load_dwordx4 s[4:7], s[0:1], 0x0
	s_load_dwordx2 s[22:23], s[0:1], 0x10
	s_load_dwordx2 s[20:21], s[0:1], 0x18
	s_load_dwordx4 s[12:15], s[0:1], 0x20
	s_load_dwordx2 s[10:11], s[0:1], 0x30
	s_and_b32 s3, s2, 7
	s_lshl_b32 s3, s3, 6
	s_lshr_b32 s16, s2, 3
	s_add_i32 s16, s16, s3
	s_lshr_b32 s18, s16, 5
	s_mov_b32 s19, 0
	s_and_b32 s28, s16, 31
	s_lshl_b32 s28, s28, 4
	s_add_i32 s29, s28, 1
	v_readfirstlane_b32 s17, v0
	v_and_b32_e32 v1, 63, v0
	v_lshlrev_b32_e32 v66, 4, v0
	s_lshr_b32 s17, s17, 6
	s_lshl_b32 s24, s17, 4
	s_lshl_b32 s30, s18, 15
	s_lshl_b32 s31, s18, 23
	v_add_u32_e32 v67, 0x1000, v66
	v_add_u32_e32 v68, 0x2000, v66
	v_add_u32_e32 v69, 0x3000, v66
	v_add_u32_e32 v70, 0x4000, v66
	v_add_u32_e32 v71, 0x5000, v66
	v_add_u32_e32 v72, 0x6000, v66
	v_add_u32_e32 v73, 0x7000, v66
	s_movk_i32 s9, 0x810
	s_mov_b32 s3, 0x8100
	s_mul_i32 s36, s29, 0x810
	v_mov_b32_e32 v141, s36
	v_sub_u32_e32 v141, 0, v141
	s_waitcnt lgkmcnt(0)
	s_add_u32 s34, s6, s30
	s_addc_u32 s35, s7, 0
	s_add_u32 s32, s4, s31
	s_addc_u32 s33, s5, 0
	global_load_dwordx4 v[74:77], v66, s[34:35]
	global_load_dwordx4 v[78:81], v67, s[34:35]
	global_load_dwordx4 v[82:85], v68, s[34:35]
	global_load_dwordx4 v[86:89], v69, s[34:35]
	global_load_dwordx4 v[90:93], v70, s[34:35]
	global_load_dwordx4 v[94:97], v71, s[34:35]
	global_load_dwordx4 v[98:101], v72, s[34:35]
	global_load_dwordx4 v[102:105], v73, s[34:35]
	v_and_b32_e32 v150, 15, v0
	v_or_b32_e32 v150, s24, v150
	v_and_b32_e32 v151, 48, v0
	v_lshl_or_b32 v150, v150, 10, v151
	global_load_dwordx4 v[62:65], v150, s[22:23] offset:0
	global_load_dwordx4 v[58:61], v150, s[22:23] offset:64
	global_load_dwordx4 v[54:57], v150, s[22:23] offset:128
	global_load_dwordx4 v[50:53], v150, s[22:23] offset:192
	global_load_dwordx4 v[46:49], v150, s[22:23] offset:256
	global_load_dwordx4 v[42:45], v150, s[22:23] offset:320
	global_load_dwordx4 v[38:41], v150, s[22:23] offset:384
	global_load_dwordx4 v[34:37], v150, s[22:23] offset:448
	global_load_dwordx4 v[30:33], v150, s[22:23] offset:512
	global_load_dwordx4 v[26:29], v150, s[22:23] offset:576
	global_load_dwordx4 v[22:25], v150, s[22:23] offset:640
	global_load_dwordx4 v[18:21], v150, s[22:23] offset:704
	global_load_dwordx4 v[14:17], v150, s[22:23] offset:768
	global_load_dwordx4 v[10:13], v150, s[22:23] offset:832
	global_load_dwordx4 v[6:9], v150, s[22:23] offset:896
	global_load_dwordx4 v[2:5], v150, s[22:23] offset:960
	v_mov_b32_e32 v142, 1
	v_mov_b32_e32 v143, 4
	v_mov_b32_e32 v144, 0x11100
	v_lshlrev_b32_e32 v145, 8, v0
	v_lshlrev_b32_e32 v148, 3, v0
	v_mov_b32_e32 v152, 0
	v_mov_b32_e32 v153, 0
	ds_write_b64 v148, v[152:153] offset:32768
	ds_write_b64 v148, v[152:153] offset:34832
	ds_write_b64 v148, v[152:153] offset:36896
	ds_write_b64 v148, v[152:153] offset:38960
	ds_write_b64 v148, v[152:153] offset:41024
	ds_write_b64 v148, v[152:153] offset:43088
	ds_write_b64 v148, v[152:153] offset:45152
	ds_write_b64 v148, v[152:153] offset:47216
	ds_write_b64 v148, v[152:153] offset:49280
	ds_write_b64 v148, v[152:153] offset:51344
	ds_write_b64 v148, v[152:153] offset:53408
	ds_write_b64 v148, v[152:153] offset:55472
	ds_write_b64 v148, v[152:153] offset:57536
	ds_write_b64 v148, v[152:153] offset:59600
	ds_write_b64 v148, v[152:153] offset:61664
	ds_write_b64 v148, v[152:153] offset:63728
	v_cmp_gt_u32_e32 vcc, 16, v0
	s_and_saveexec_b64 s[30:31], vcc
	v_mul_u32_u24_e32 v151, 0x810, v0
	ds_write_b64 v151, v[152:153] offset:34816
	v_mov_b32_e32 v150, 0x11540
	v_mov_b32_e32 v149, 8
	ds_write_b32 v150, v149
	s_mov_b64 exec, s[30:31]
	v_cmp_gt_u32_e32 vcc, 64, v0
	s_and_saveexec_b64 s[30:31], vcc
	v_mov_b32_e32 v150, 0x11600
	v_lshl_add_u32 v150, v0, 2, v150
	ds_write_b32 v150, v152
	s_mov_b64 exec, s[30:31]
	s_waitcnt lgkmcnt(0)
	s_barrier
	s_waitcnt vmcnt(16)
	v_mad_u32_u24 v74, v74, s9, v141
	v_mad_u32_u24 v75, v75, s9, v141
	v_mad_u32_u24 v76, v76, s9, v141
	v_mad_u32_u24 v77, v77, s9, v141
	v_mad_u32_u24 v78, v78, s9, v141
	v_mad_u32_u24 v79, v79, s9, v141
	v_mad_u32_u24 v80, v80, s9, v141
	v_mad_u32_u24 v81, v81, s9, v141
	v_mad_u32_u24 v82, v82, s9, v141
	v_mad_u32_u24 v83, v83, s9, v141
	v_mad_u32_u24 v84, v84, s9, v141
	v_mad_u32_u24 v85, v85, s9, v141
	v_mad_u32_u24 v86, v86, s9, v141
	v_mad_u32_u24 v87, v87, s9, v141
	v_mad_u32_u24 v88, v88, s9, v141
	v_mad_u32_u24 v89, v89, s9, v141
	v_mad_u32_u24 v90, v90, s9, v141
	v_mad_u32_u24 v91, v91, s9, v141
	v_mad_u32_u24 v92, v92, s9, v141
	v_mad_u32_u24 v93, v93, s9, v141
	v_mad_u32_u24 v94, v94, s9, v141
	v_mad_u32_u24 v95, v95, s9, v141
	v_mad_u32_u24 v96, v96, s9, v141
	v_mad_u32_u24 v97, v97, s9, v141
	v_mad_u32_u24 v98, v98, s9, v141
	v_mad_u32_u24 v99, v99, s9, v141
	v_mad_u32_u24 v100, v100, s9, v141
	v_mad_u32_u24 v101, v101, s9, v141
	v_mad_u32_u24 v102, v102, s9, v141
	v_mad_u32_u24 v103, v103, s9, v141
	v_mad_u32_u24 v104, v104, s9, v141
	v_mad_u32_u24 v105, v105, s9, v141
	v_cmp_gt_u32_e64 s[36:37], s3, v74
	v_cmp_gt_u32_e64 s[38:39], s3, v75
	v_cmp_gt_u32_e64 s[40:41], s3, v76
	v_cmp_gt_u32_e64 s[42:43], s3, v77
	v_cmp_gt_u32_e64 s[44:45], s3, v78
	v_cmp_gt_u32_e64 s[46:47], s3, v79
	v_cmp_gt_u32_e64 s[48:49], s3, v80
	v_cmp_gt_u32_e64 s[50:51], s3, v81
	v_cmp_gt_u32_e64 s[52:53], s3, v82
	v_cmp_gt_u32_e64 s[54:55], s3, v83
	v_cmp_gt_u32_e64 s[56:57], s3, v84
	v_cmp_gt_u32_e64 s[58:59], s3, v85
	v_cmp_gt_u32_e64 s[60:61], s3, v86
	v_cmp_gt_u32_e64 s[62:63], s3, v87
	v_cmp_gt_u32_e64 s[64:65], s3, v88
	v_cmp_gt_u32_e64 s[66:67], s3, v89
	v_cmp_gt_u32_e64 s[68:69], s3, v90
	v_cmp_gt_u32_e64 s[70:71], s3, v91
	v_cmp_gt_u32_e64 s[72:73], s3, v92
	v_cmp_gt_u32_e64 s[74:75], s3, v93
	v_cmp_gt_u32_e64 s[76:77], s3, v94
	v_cmp_gt_u32_e64 s[78:79], s3, v95
	v_cmp_gt_u32_e64 s[80:81], s3, v96
	v_cmp_gt_u32_e64 s[82:83], s3, v97
	v_cmp_gt_u32_e64 s[84:85], s3, v98
	v_cmp_gt_u32_e64 s[86:87], s3, v99
	v_cmp_gt_u32_e64 s[88:89], s3, v100
	v_cmp_gt_u32_e64 s[90:91], s3, v101
	v_cmp_gt_u32_e64 s[92:93], s3, v102
	v_cmp_gt_u32_e64 s[94:95], s3, v103
	v_cmp_gt_u32_e64 s[96:97], s3, v104
	v_cmp_gt_u32_e64 s[98:99], s3, v105
	s_mov_b64 exec, s[36:37]
	ds_add_u32 v74, v142 offset:34816
	s_mov_b64 exec, s[38:39]
	ds_add_u32 v75, v142 offset:34816
	s_mov_b64 exec, s[40:41]
	ds_add_u32 v76, v142 offset:34816
	s_mov_b64 exec, s[42:43]
	ds_add_u32 v77, v142 offset:34816
	s_mov_b64 exec, s[44:45]
	ds_add_u32 v78, v142 offset:34816
	s_mov_b64 exec, s[46:47]
	ds_add_u32 v79, v142 offset:34816
	s_mov_b64 exec, s[48:49]
	ds_add_u32 v80, v142 offset:34816
	s_mov_b64 exec, s[50:51]
	ds_add_u32 v81, v142 offset:34816
	s_mov_b64 exec, s[52:53]
	ds_add_u32 v82, v142 offset:34816
	s_mov_b64 exec, s[54:55]
	ds_add_u32 v83, v142 offset:34816
	s_mov_b64 exec, s[56:57]
	ds_add_u32 v84, v142 offset:34816
	s_mov_b64 exec, s[58:59]
	ds_add_u32 v85, v142 offset:34816
	s_mov_b64 exec, s[60:61]
	ds_add_u32 v86, v142 offset:34816
	s_mov_b64 exec, s[62:63]
	ds_add_u32 v87, v142 offset:34816
	s_mov_b64 exec, s[64:65]
	ds_add_u32 v88, v142 offset:34816
	s_mov_b64 exec, s[66:67]
	ds_add_u32 v89, v142 offset:34816
	s_mov_b64 exec, s[68:69]
	ds_add_u32 v90, v142 offset:34816
	s_mov_b64 exec, s[70:71]
	ds_add_u32 v91, v142 offset:34816
	s_mov_b64 exec, s[72:73]
	ds_add_u32 v92, v142 offset:34816
	s_mov_b64 exec, s[74:75]
	ds_add_u32 v93, v142 offset:34816
	s_mov_b64 exec, s[76:77]
	ds_add_u32 v94, v142 offset:34816
	s_mov_b64 exec, s[78:79]
	ds_add_u32 v95, v142 offset:34816
	s_mov_b64 exec, s[80:81]
	ds_add_u32 v96, v142 offset:34816
	s_mov_b64 exec, s[82:83]
	ds_add_u32 v97, v142 offset:34816
	s_mov_b64 exec, s[84:85]
	ds_add_u32 v98, v142 offset:34816
	s_mov_b64 exec, s[86:87]
	ds_add_u32 v99, v142 offset:34816
	s_mov_b64 exec, s[88:89]
	ds_add_u32 v100, v142 offset:34816
	s_mov_b64 exec, s[90:91]
	ds_add_u32 v101, v142 offset:34816
	s_mov_b64 exec, s[92:93]
	ds_add_u32 v102, v142 offset:34816
	s_mov_b64 exec, s[94:95]
	ds_add_u32 v103, v142 offset:34816
	s_mov_b64 exec, s[96:97]
	ds_add_u32 v104, v142 offset:34816
	s_mov_b64 exec, s[98:99]
	ds_add_u32 v105, v142 offset:34816
	s_mov_b64 exec, -1
	s_waitcnt lgkmcnt(0)
	s_barrier
	v_and_b32_e32 v67, 15, v0
	v_mul_u32_u24_e32 v67, 0x810, v67
	ds_read_b32 v68, v67 offset:34816
	s_waitcnt lgkmcnt(0)
	v_mov_b32_e32 v69, v68
	s_nop 1
	v_add_u32_dpp v69, v69, v69 row_shr:1 row_mask:0xf bank_mask:0xf bound_ctrl:1
	s_nop 1
	v_add_u32_dpp v69, v69, v69 row_shr:2 row_mask:0xf bank_mask:0xf bound_ctrl:1
	s_nop 1
	v_add_u32_dpp v69, v69, v69 row_shr:4 row_mask:0xf bank_mask:0xf bound_ctrl:1
	s_nop 1
	v_add_u32_dpp v69, v69, v69 row_shr:8 row_mask:0xf bank_mask:0xf bound_ctrl:1
	s_nop 1
	v_sub_u32_e32 v70, v69, v68
	v_lshlrev_b32_e32 v70, 2, v70
	v_readlane_b32 s8, v69, 15
	s_cmp_lg_u32 s17, 0
	s_cbranch_scc1 .Lfront_nocursor
	v_cmp_gt_u32_e32 vcc, 16, v1
	s_and_saveexec_b64 s[30:31], vcc
	ds_write_b32 v67, v70 offset:34820
	s_mov_b64 exec, s[30:31]

.Lg_nocopy:
	v_mov_b32_e32 v97, 1
	v_and_b32_e32 v138, 15, v0
	v_or_b32_e32 v134, s24, v138
	v_lshlrev_b32_e32 v135, 3, v1
	v_lshlrev_b32_e32 v139, 2, v1
	v_bfe_u32 v140, v0, 4, 2
	v_cmp_eq_u32_e64 s[2:3], 0, v1

.LBB0_148:
	s_mov_b32 s92, s22
	s_mov_b32 s93, s8
	s_mov_b32 s94, s0
	s_mov_b32 s95, s4
	s_ashr_i32 s23, s22, 31
	s_lshl_b64 s[6:7], s[22:23], 10
	s_ashr_i32 s9, s8, 31
	v_lshl_add_u64 v[4:5], v[2:3], 0, s[6:7]
	s_lshl_b64 s[6:7], s[8:9], 10
	s_ashr_i32 s1, s0, 31
	v_lshl_add_u64 v[6:7], v[2:3], 0, s[6:7]
	s_lshl_b64 s[6:7], s[0:1], 10
	s_ashr_i32 s5, s4, 31
	global_load_dwordx4 v[14:17], v[4:5], off
	global_load_dwordx4 v[10:13], v[6:7], off
	v_lshl_add_u64 v[20:21], v[2:3], 0, s[6:7]
	s_lshl_b64 s[6:7], s[4:5], 10
	v_lshl_add_u64 v[22:23], v[2:3], 0, s[6:7]
	global_load_dwordx4 v[6:9], v[20:21], off
	global_load_dwordx4 v[2:5], v[22:23], off
	s_mul_i32 s1, s17, 0x1020
	v_mov_b32_e32 v19, 0
	v_lshl_add_u32 v1, v1, 2, s1
	v_lshl_add_u64 v[20:21], s[20:21], 0, v[18:19]
	v_add_u32_e32 v18, 8, v1
	v_add_u32_e32 v22, 16, v1
	ds_read2st64_b32 v[36:37], v1 offset1:1
	ds_read2st64_b32 v[34:35], v1 offset0:2 offset1:3
	v_add_u32_e32 v1, 24, v1
	ds_read2st64_b32 v[32:33], v18 offset0:4 offset1:5
	ds_read2st64_b32 v[30:31], v18 offset0:6 offset1:7
	ds_read2st64_b32 v[28:29], v22 offset0:8 offset1:9
	ds_read2st64_b32 v[26:27], v22 offset0:10 offset1:11
	ds_read2st64_b32 v[24:25], v1 offset0:12 offset1:13
	ds_read2st64_b32 v[22:23], v1 offset0:14 offset1:15
	s_lshl_b32 s5, s18, 9
	s_or_b32 s1, s5, s28
	s_waitcnt lgkmcnt(7)
	v_add_f32_e64 v1, |v36|, |v37|
	s_mov_b32 s7, 0
	s_add_i32 s6, s1, s29
	s_waitcnt lgkmcnt(6)
	v_add_f32_e64 v1, |v34|, v1
	s_lshl_b64 s[18:19], s[6:7], 10
	v_add_f32_e64 v1, |v35|, v1
	v_lshl_add_u64 v[42:43], v[20:21], 0, s[18:19]
	v_cmp_lt_f32_e32 vcc, 0, v1
	s_waitcnt vmcnt(3)
	v_pk_add_f32 v[38:39], v[14:15], v[36:37] neg_lo:[0,1] neg_hi:[0,1]
	v_pk_add_f32 v[40:41], v[16:17], v[34:35] neg_lo:[0,1] neg_hi:[0,1]
	v_pk_add_f32 v[38:39], v[36:37], v[38:39]
	v_pk_add_f32 v[40:41], v[34:35], v[40:41]
	global_store_dwordx4 v[42:43], v[38:41], off nt
	s_cbranch_vccz .LBB0_150
	v_pk_add_f32 v[14:15], v[36:37], v[14:15] neg_lo:[0,1] neg_hi:[0,1]
	v_pk_add_f32 v[16:17], v[34:35], v[16:17] neg_lo:[0,1] neg_hi:[0,1]
	v_pk_mul_f32 v[14:15], v[14:15], v[14:15]
	v_pk_mul_f32 v[16:17], v[16:17], v[16:17]
	v_add_f32_e32 v1, v14, v15
	v_add_f32_e32 v1, v1, v16
	v_add_f32_e32 v19, v1, v17
	s_mov_b32 s7, 1

.LBB0_166:
	s_or_b64 exec, exec, s[0:1]
	s_mov_b64 exec, 1
	s_lshl_b32 s96, s92, 2
	s_add_i32 s96, s96, 0x11600
	v_mov_b32_e32 v70, s96
	ds_add_u32 v70, v97
	s_lshl_b32 s96, s93, 2
	s_add_i32 s96, s96, 0x11600
	v_mov_b32_e32 v70, s96
	ds_add_u32 v70, v97
	s_lshl_b32 s96, s94, 2
	s_add_i32 s96, s96, 0x11600
	v_mov_b32_e32 v70, s96
	ds_add_u32 v70, v97
	s_lshl_b32 s96, s95, 2
	s_add_i32 s96, s96, 0x11600
	v_mov_b32_e32 v70, s96
	ds_add_u32 v70, v97
	s_mov_b64 exec, -1
	v_cmp_gt_u32_e32 vcc, 64, v0
	s_waitcnt lgkmcnt(0)
	s_barrier
	s_and_saveexec_b64 s[0:1], vcc
	s_cbranch_execnz .LBB0_169
	s_or_b64 exec, exec, s[0:1]
	v_cmp_eq_u32_e32 vcc, 64, v0
	s_and_saveexec_b64 s[0:1], vcc
	s_cbranch_execnz .LBB0_170

.LBB0_169:
	v_mov_b32_e32 v1, 0x11600
	v_lshl_add_u32 v1, v0, 2, v1
	ds_read_b32 v1, v1
	s_waitcnt lgkmcnt(0)
	v_lshl_add_u32 v2, v0, 9, s16
	global_store_byte v2, v1, s[12:13]
	s_or_b64 exec, exec, s[0:1]
	v_cmp_eq_u32_e32 vcc, 64, v0
	s_and_saveexec_b64 s[0:1], vcc
	s_cbranch_execz .LBB0_168
